# grid barriers 8 and 9 (out-proj -> postmix -> q_route) replaced by per-row-tile hand-offs among the 8 same-XCD workgroups owning the tile (virtual block id = xcc_id + 8*rank from the census; falls bac
# speedup vs baseline: 1.0097x; 1.0097x over previous
; #define LAS __attribute__((address_space(3)))
; __device__ __forceinline__ unsigned xb_add(unsigned* p, unsigned v) { return __hip_atomic_fetch_add(p, v, __ATOMIC_RELAXED, __HIP_MEMORY_SCOPE_AGENT); }
; __device__ __forceinline__ unsigned xb_xcc_id() { return (unsigned)__builtin_amdgcn_s_getreg((3 << 11) | 20) & 0xFu; }
; __device__ __forceinline__ XcdBarrier xcd_barrier_post(unsigned* bar, volatile LAS unsigned* st) {
;   XcdBarrier b; b.bar = bar; b.x = xb_xcc_id(); b.st = st;
;   if (threadIdx.x == 0) (void)xb_add(&bar[XB_XCNT(b.x)], 1u);
;   return b;
; }
; __global__ void __launch_bounds__(NTHREADS, 2) fwd_mega(Params p_unused) {
;     ...
;   volatile LAS unsigned* st = (volatile LAS unsigned*)(smem + 75792);
;   if (threadIdx.x == 0) { st[0] = 0u; st[1] = 0u; }
;   __syncthreads();
;   KParams* kp0 = (KParams*)__builtin_amdgcn_kernarg_segment_ptr();
;     ...
;   XcdBarrier bar;
;   PHASE(bar = xcd_barrier_post(p.bar, st))
.LBB0_2:
	s_or_b64 exec, exec, s[6:7]
	s_mov_b64 s[6:7], s[0:1]
	s_waitcnt lgkmcnt(0)
	s_barrier
	s_load_dwordx2 s[44:45], s[6:7], 0x220
	s_getreg_b32 s3, hwreg(HW_REG_XCC_ID, 0, 4)
	s_and_b32 s33, s3, 15
	s_and_saveexec_b64 s[6:7], s[4:5]
	s_cbranch_execz .LBB0_5
	s_mov_b64 s[8:9], exec
	v_mbcnt_lo_u32_b32 v1, s8, 0
	v_mbcnt_hi_u32_b32 v1, s9, v1
	v_cmp_eq_u32_e32 vcc, 0, v1
	s_and_b64 s[10:11], exec, vcc
	s_mov_b64 exec, s[10:11]
	s_cbranch_execz .LBB0_5
	s_lshl_b32 s3, s33, 8
	s_bcnt1_i32_b64 s8, s[8:9]
	v_mov_b32_e32 v1, s3
	v_mov_b32_e32 v2, s8
	s_waitcnt lgkmcnt(0)
	global_atomic_add v254, v1, v2, s[44:45] offset:1024 sc0
	s_mov_b32 s98, 0

; __device__ __forceinline__ unsigned xb_ld(unsigned* p)              { return __hip_atomic_load(p, __ATOMIC_RELAXED, __HIP_MEMORY_SCOPE_AGENT); }
; __device__ __forceinline__ void xcd_barrier_complete(unsigned* bar, unsigned x, unsigned& nloc, unsigned& nx) {
;   const unsigned G = gridDim.x * gridDim.y * gridDim.z;
;   unsigned sum, cnt, mine, sp = 0u;
;   for (;;) {
;     sum = 0u; cnt = 0u; mine = 0u;
; #pragma unroll
;     for (unsigned j = 0; j < 16; ++j) { const unsigned c = xb_ld(&bar[XB_XCNT(j)]); sum += c; cnt += (c > 0u) ? 1u : 0u; mine = (j == x) ? c : mine; }
;     if (sum == G) break;
;     __builtin_amdgcn_s_sleep(1);
;     if ((++sp & 255u) == 0u) { if (xb_ld(&bar[XB_TMO])) break; if (sp > XB_SPIN_CAP) { atomicAdd(&bar[XB_TMO], 1u); break; } }
;   }
;   nloc = mine > 0u ? mine : 1u; nx = cnt > 0u ? cnt : 1u;
; }
.LBB0_71:
	s_cmp_eq_u32 s33, 0
	s_cselect_b64 vcc, -1, 0
	s_cmp_eq_u32 s33, 1
	v_cndmask_b32_e32 v17, 0, v16, vcc
	s_cselect_b64 vcc, -1, 0
	s_cmp_eq_u32 s33, 2
	v_cndmask_b32_e32 v17, v17, v1, vcc
	s_cselect_b64 vcc, -1, 0
	s_cmp_eq_u32 s33, 3
	v_cndmask_b32_e32 v17, v17, v2, vcc
	s_cselect_b64 vcc, -1, 0
	s_cmp_eq_u32 s33, 4
	v_cndmask_b32_e32 v17, v17, v3, vcc
	s_cselect_b64 vcc, -1, 0
	s_cmp_eq_u32 s33, 5
	v_cndmask_b32_e32 v17, v17, v4, vcc
	s_cselect_b64 vcc, -1, 0
	s_cmp_eq_u32 s33, 6
	v_cndmask_b32_e32 v17, v17, v5, vcc
	s_cselect_b64 vcc, -1, 0
	s_cmp_eq_u32 s33, 7
	v_cndmask_b32_e32 v17, v17, v6, vcc
	s_cselect_b64 vcc, -1, 0
	s_cmp_eq_u32 s33, 8
	v_cndmask_b32_e32 v17, v17, v7, vcc
	s_cselect_b64 vcc, -1, 0
	s_cmp_eq_u32 s33, 9
	v_cndmask_b32_e32 v17, v17, v8, vcc
	s_cselect_b64 vcc, -1, 0
	s_cmp_eq_u32 s33, 10
	v_cndmask_b32_e32 v17, v17, v9, vcc
	s_cselect_b64 vcc, -1, 0
	s_cmp_eq_u32 s33, 11
	v_cndmask_b32_e32 v17, v17, v10, vcc
	s_cselect_b64 vcc, -1, 0
	s_cmp_eq_u32 s33, 12
	v_cndmask_b32_e32 v17, v17, v11, vcc
	s_cselect_b64 vcc, -1, 0
	s_cmp_eq_u32 s33, 13
	v_cndmask_b32_e32 v17, v17, v12, vcc
	s_cselect_b64 vcc, -1, 0
	s_cmp_eq_u32 s33, 14
	v_cndmask_b32_e32 v17, v17, v13, vcc
	s_cselect_b64 vcc, -1, 0
	s_cmp_eq_u32 s33, 15
	v_cndmask_b32_e32 v17, v17, v14, vcc
	s_cselect_b64 vcc, -1, 0
	v_cndmask_b32_e32 v17, v17, v15, vcc
	v_xor_b32_e32 v18, 64, v16
	v_xor_b32_e32 v19, 64, v1
	v_or_b32_e32 v18, v18, v19
	v_xor_b32_e32 v19, 64, v2
	v_or_b32_e32 v18, v18, v19
	v_xor_b32_e32 v19, 64, v3
	v_or_b32_e32 v18, v18, v19
	v_xor_b32_e32 v19, 64, v4
	v_or_b32_e32 v18, v18, v19
	v_xor_b32_e32 v19, 64, v5
	v_or_b32_e32 v18, v18, v19
	v_xor_b32_e32 v19, 64, v6
	v_or_b32_e32 v18, v18, v19
	v_xor_b32_e32 v19, 64, v7
	v_or_b32_e32 v18, v18, v19
	v_mov_b32_e32 v19, s34
	v_xor_b32_e32 v19, 0x200, v19
	v_or_b32_e32 v18, v18, v19
	v_lshl_add_u32 v19, v254, 3, s33
	v_cmp_eq_u32_e32 vcc, 0, v18
	v_mov_b32_e32 v20, s2
	s_nop 1
	v_cndmask_b32_e32 v19, v20, v19, vcc
	v_mov_b32_e32 v20, 0x12818
	ds_write_b32 v20, v19
	ds_write_b32 v20, v18 offset:4
	v_cmp_ne_u32_e32 vcc, 0, v16
	s_nop 1
	v_cndmask_b32_e64 v16, 0, 1, vcc
	v_cmp_ne_u32_e32 vcc, 0, v1
	s_nop 1
	v_addc_co_u32_e32 v1, vcc, 0, v16, vcc
	v_cmp_ne_u32_e32 vcc, 0, v2
	s_nop 1
	v_cndmask_b32_e64 v2, 0, 1, vcc
	v_cmp_ne_u32_e32 vcc, 0, v3
	v_max_u32_e32 v3, 1, v17
	s_nop 0
	v_addc_co_u32_e32 v1, vcc, v1, v2, vcc
	v_cmp_ne_u32_e32 vcc, 0, v4
	s_nop 1
	v_cndmask_b32_e64 v2, 0, 1, vcc
	v_cmp_ne_u32_e32 vcc, 0, v5
	s_nop 1
	v_addc_co_u32_e32 v1, vcc, v1, v2, vcc
	v_cmp_ne_u32_e32 vcc, 0, v6
	s_nop 1
	v_cndmask_b32_e64 v2, 0, 1, vcc
	v_cmp_ne_u32_e32 vcc, 0, v7
	s_nop 1
	v_addc_co_u32_e32 v1, vcc, v1, v2, vcc
	v_cmp_ne_u32_e32 vcc, 0, v8
	s_nop 1
	v_cndmask_b32_e64 v2, 0, 1, vcc
	v_cmp_ne_u32_e32 vcc, 0, v9
	s_nop 1
	v_addc_co_u32_e32 v1, vcc, v1, v2, vcc
	v_cmp_ne_u32_e32 vcc, 0, v10
	s_nop 1
	v_cndmask_b32_e64 v2, 0, 1, vcc
	v_cmp_ne_u32_e32 vcc, 0, v11
	s_nop 1
	v_addc_co_u32_e32 v1, vcc, v1, v2, vcc
	v_cmp_ne_u32_e32 vcc, 0, v12
	s_nop 1
	v_cndmask_b32_e64 v2, 0, 1, vcc
	v_cmp_ne_u32_e32 vcc, 0, v13
	s_nop 1
	v_addc_co_u32_e32 v1, vcc, v1, v2, vcc
	v_cmp_ne_u32_e32 vcc, 0, v14
	s_nop 1
	v_cndmask_b32_e64 v2, 0, 1, vcc
	v_cmp_ne_u32_e32 vcc, 0, v15
	s_nop 1
	v_addc_co_u32_e32 v1, vcc, v1, v2, vcc
	v_mov_b32_e32 v2, 0x12810
	v_max_u32_e32 v1, 1, v1
	ds_write_b32 v2, v3
	v_mov_b32_e32 v2, 0x12814
	ds_write_b32 v2, v1

; __device__ void phase_outproj(KParams& p, int bid, int nb, char* smem) {
;   const bool aware = (nb & 7) == 0;
;   const int start = aware ? (bid >> 3) : bid, step = aware ? (nb >> 3) : nb, end = aware ? 64 : 512;
;   const bf16_t* a8 = reinterpret_cast<const bf16_t*>(p.ycat8);
;   const bf16_t* b8 = reinterpret_cast<const bf16_t*>(p.wo8);
;   for (int it = start; it < end; it += step) {
;     const int x = aware ? (bid & 7) : (it >> 6), s_ = aware ? it : (it & 63);
;     EpiBf16 epi{reinterpret_cast<bf16_t*>(p.y_x), D};
;     gemm_tile_n256<true>(a8, D / 2, b8, D / 2, D / 2, (8 * x + (s_ & 7)) * 128, (s_ >> 3) * 256, epi, smem, p.yscale, p.woscale);
.Lgb_wd_7:
.LBB0_1067:
	s_or_b64 exec, exec, s[12:13]
	v_mov_b32_e32 v253, 0x12818
	ds_read_b32 v253, v253
	s_waitcnt lgkmcnt(0)
	v_readfirstlane_b32 s99, v253
	s_nop 0
	s_and_b64 s[100:101], s[48:49], exec
	s_cbranch_scc0 .Lmy_op_na
	s_lshr_b32 s3, s99, 3
.Lmy_op_na:
	s_and_b64 s[12:13], s[48:49], exec
	s_cselect_b32 s42, 64, 0x200
	s_mov_b64 s[20:21], s[0:1]
	s_cmp_ge_i32 s3, s42
	s_waitcnt lgkmcnt(0)
	s_barrier
	s_cbranch_scc1 .LBB0_1072
	s_load_dwordx8 s[12:19], s[20:21], 0x118
	s_movk_i32 s46, 0x80
	s_load_dwordx2 s[20:21], s[20:21], 0x230
	s_and_b32 s43, s99, 7
	v_and_or_b32 v1, v1, 12, v193
	v_and_or_b32 v135, v183, s46, v185
	s_mov_b32 s47, 0x1ffffc0
	s_mov_b64 s[22:23], 0x10000
	s_mov_b64 s[24:25], 0x20000
	s_mov_b64 s[26:27], 0x30000
	s_mov_b64 s[28:29], 0x40000
	s_mov_b64 s[30:31], 0x50000
	s_mov_b64 s[36:37], 0x60000
	s_mov_b64 s[38:39], 0x70000

; __device__ __forceinline__ unsigned xb_ld(unsigned* p)              { return __hip_atomic_load(p, __ATOMIC_RELAXED, __HIP_MEMORY_SCOPE_AGENT); }
; __device__ __forceinline__ unsigned xb_add(unsigned* p, unsigned v) { return __hip_atomic_fetch_add(p, v, __ATOMIC_RELAXED, __HIP_MEMORY_SCOPE_AGENT); }
; #define XB_SPIN(cond, bar) do { unsigned _sp = 0; while (cond) { __builtin_amdgcn_s_sleep(1); \
;     if ((++_sp & 255u) == 0u) { if (xb_ld(&(bar)[XB_TMO])) break; if (_sp > XB_SPIN_CAP) { atomicAdd(&(bar)[XB_TMO], 1u); break; } } } } while (0)
; __device__ __forceinline__ void xcd_barrier(const XcdBarrier& b) {
;   asm volatile("s_waitcnt vmcnt(0)" ::: "memory");
;   __syncthreads();
;   if (threadIdx.x == 0) {
;     unsigned* bar = b.bar;
;     __builtin_amdgcn_s_waitcnt(0);
;     unsigned nloc = b.st[0], nx = b.st[1];
;     if (nloc == 0u) { xcd_barrier_complete(bar, b.x, nloc, nx); b.st[0] = nloc; b.st[1] = nx; }
;     const unsigned old = xb_add(&bar[XB_XSUB(b.x)], 1u);
;     const unsigned gen = old / nloc;
;     if (old + 1u == (gen + 1u) * nloc) {
;       __builtin_amdgcn_fence(__ATOMIC_RELEASE, "agent");
;       asm volatile("s_waitcnt vmcnt(0)" ::: "memory");
;       const unsigned og = xb_add(&bar[XB_TOP], 1u);
;       const unsigned tg = og / nx;
;       if (og + 1u == (tg + 1u) * nx) xb_add(&bar[XB_TOPGEN], 1u);
;       else XB_SPIN(xb_ld(&bar[XB_TOPGEN]) == tg, bar);
;       __builtin_amdgcn_fence(__ATOMIC_ACQUIRE, "agent");
;       xb_add(&bar[XB_XGEN(b.x)], 1u);
;       asm volatile("s_waitcnt vmcnt(0)" ::: "memory");
;     } else {
;       XB_SPIN(xb_ld(&bar[XB_XGEN(b.x)]) == gen, bar);
;       __builtin_amdgcn_fence(__ATOMIC_ACQUIRE, "agent");
;       asm volatile("s_waitcnt vmcnt(0)" ::: "memory");
;     }
;   }
;   __syncthreads();
; }
.LBB0_1072:
	s_waitcnt vmcnt(0)
	s_waitcnt vmcnt(63) expcnt(7) lgkmcnt(15)
	s_barrier
	s_and_saveexec_b64 s[12:13], s[4:5]
	s_cbranch_execz .LBB0_1124
	s_waitcnt vmcnt(0) lgkmcnt(0)
	v_mov_b32_e32 v253, 0x12818
	ds_read_b32 v254, v253 offset:4
	ds_read_b32 v253, v253
	s_waitcnt lgkmcnt(0)
	v_cmp_ne_u32_e32 vcc, 0, v254
	s_cbranch_vccnz .Lmy_gbar_8
	v_readfirstlane_b32 s99, v253
	s_nop 0
	s_and_b32 s100, s99, 7
	s_bfe_u32 s101, s99, 0x30003
	s_lshl_b32 s100, s100, 3
	s_or_b32 s100, s100, s101
	s_and_b32 s101, s100, 31
	s_add_u32 s101, s101, 12
	s_lshl_b32 s101, s101, 8
	s_lshr_b32 s100, s100, 5
	s_lshl_b32 s100, s100, 6
	s_add_u32 s101, s101, s100
	v_mov_b32_e32 v253, s101
	v_mov_b32_e32 v254, 1
	global_atomic_add v253, v254, s[44:45] offset:128
	buffer_inv sc1
	s_mov_b32 s100, 0
.Lmy_gs_w_8:
	global_load_dword v254, v253, s[44:45] offset:128 sc1
	s_waitcnt vmcnt(0)
	v_cmp_le_u32_e32 vcc, 8, v254
	s_cbranch_vccnz .Lgb_wd_8
	s_sleep 1
	s_add_u32 s100, s100, 1
	s_cmp_lt_u32 s100, 0x100000
	s_cbranch_scc1 .Lmy_gs_w_8
	s_branch .Lgb_wd_8
.Lmy_gbar_8:
	s_add_u32 s98, s98, 1
	v_mov_b32_e32 v253, 0x12810
	ds_read_b32 v254, v253
	ds_read_b32 v253, v253 offset:4
	s_lshl_b32 s101, s33, 8
	s_add_u32 s99, s101, 5120
	s_waitcnt lgkmcnt(0)
	v_readfirstlane_b32 s100, v254
	v_mov_b32_e32 v254, s99
	v_readfirstlane_b32 s99, v253
	s_nop 0
	v_mov_b32_e32 v253, v254
	v_mov_b32_e32 v254, 1
	global_atomic_add v254, v253, v254, s[44:45] offset:64 sc0
	buffer_inv sc1
	s_mul_i32 s100, s100, s98
	s_mul_i32 s99, s99, s98
	s_waitcnt vmcnt(0)
	v_add_u32_e32 v254, 1, v254
	v_cmp_ne_u32_e32 vcc, s100, v254
	s_cbranch_vccnz .Lgb_wait_8
	buffer_wbl2 sc1
	s_waitcnt vmcnt(0)
	v_mov_b32_e32 v254, 1
	v_mov_b32_e32 v253, 9216
	global_atomic_add v253, v254, s[44:45] offset:64
	global_atomic_add v253, v254, s[44:45] offset:320
	global_atomic_add v253, v254, s[44:45] offset:576
	global_atomic_add v253, v254, s[44:45] offset:832
	global_atomic_add v253, v254, s[44:45] offset:1088
	global_atomic_add v253, v254, s[44:45] offset:1344
	global_atomic_add v253, v254, s[44:45] offset:1600
	global_atomic_add v253, v254, s[44:45] offset:1856
	v_mov_b32_e32 v253, 11264
	global_atomic_add v253, v254, s[44:45] offset:64
	global_atomic_add v253, v254, s[44:45] offset:320
	global_atomic_add v253, v254, s[44:45] offset:576
	global_atomic_add v253, v254, s[44:45] offset:832
	global_atomic_add v253, v254, s[44:45] offset:1088
	global_atomic_add v253, v254, s[44:45] offset:1344
	global_atomic_add v253, v254, s[44:45] offset:1600
	global_atomic_add v253, v254, s[44:45] offset:1856

; __device__ __forceinline__ float bflo(uint32_t w) { return __uint_as_float(w << 16); }
; __device__ __forceinline__ float bfhi(uint32_t w) { return __uint_as_float(w & 0xffff0000u); }
; __device__ void phase_postmix(KParams& p, int bid, int nb, char* smem) {
;   const int lane = threadIdx.x & 63, w = threadIdx.x >> 6;
;   for (int t = bid * 4 + w; t < T; t += nb * 4) {
;     const int b = t / L;
;     float4 y[8];
;     float ss = 0.f;
; #pragma unroll
;     for (int c = 0; c < 8; ++c) {
;       {
;         const uint2 yq = *reinterpret_cast<const uint2*>(reinterpret_cast<const bf16_t*>(p.y_x) + (size_t)t * D + c * 256 + lane * 4);
;         y[c] = float4{bflo(yq.x), bfhi(yq.x), bflo(yq.y), bfhi(yq.y)};
;       }
;       ss += y[c].x * y[c].x + y[c].y * y[c].y + y[c].z * y[c].z + y[c].w * y[c].w;
;     }
;     ss = wave_sum_fast(ss);
;     const float rstd = rsqrtf(ss * (1.f / D) + EPS);
;     const float* gm = p.mod + (size_t)b * NMOD + 2 * D;
;     float ss1 = 0.f;
; #pragma unroll
;     for (int c = 0; c < 8; ++c) {
;       const int e0 = c * 256 + lane * 4;
;       const float4 xv = *reinterpret_cast<const float4*>(p.x + (size_t)t * D + e0);
;       const float4 g4 = *reinterpret_cast<const float4*>(gm + e0), gp = *reinterpret_cast<const float4*>(p.g_post_mix + e0);
;       y[c].x = xv.x + g4.x * (y[c].x * rstd * gp.x); y[c].y = xv.y + g4.y * (y[c].y * rstd * gp.y);
;       y[c].z = xv.z + g4.z * (y[c].z * rstd * gp.z); y[c].w = xv.w + g4.w * (y[c].w * rstd * gp.w);
;       ss1 += y[c].x * y[c].x + y[c].y * y[c].y + y[c].z * y[c].z + y[c].w * y[c].w;
;     }
;     if (lane == 0) p.partial[t] = rstd;
.Lgb_wd_8:
.LBB0_1124:
	s_or_b64 exec, exec, s[12:13]
	v_mov_b32_e32 v253, 0x12818
	ds_read_b32 v253, v253
	s_waitcnt lgkmcnt(0)
	v_readfirstlane_b32 s99, v253
	s_nop 0
	s_and_b32 s100, s99, 7
	s_bfe_u32 s101, s99, 0x30003
	s_lshl_b32 s100, s100, 3
	s_or_b32 s100, s100, s101
	s_lshl_b32 s100, s100, 7
	s_lshr_b32 s101, s99, 6
	s_lshl_b32 s101, s101, 4
	s_add_u32 s100, s100, s101
	v_lshrrev_b32_e32 v210, 6, v0
	v_lshl_add_u32 v210, v210, 2, s100
	v_mov_b32_e32 v211, 0
	s_mov_b64 s[24:25], s[0:1]
	s_waitcnt lgkmcnt(0)
	s_barrier
	s_and_saveexec_b64 s[20:21], s[6:7]
	s_cbranch_execz .LBB0_1131
	s_load_dwordx2 s[26:27], s[24:25], 0x230
	s_load_dwordx4 s[12:15], s[24:25], 0x180
	s_load_dwordx2 s[28:29], s[24:25], 0xf8
	s_load_dwordx2 s[30:31], s[24:25], 0x0
	s_load_dwordx4 s[16:19], s[24:25], 0x38
	s_load_dwordx2 s[36:37], s[24:25], 0x118
	s_load_dwordx2 s[22:23], s[24:25], 0x108
	v_mov_b32_e32 v135, 0
	v_or_b32_e32 v8, 0x400, v190
	v_lshlrev_b32_e32 v10, 2, v8
	v_mov_b32_e32 v11, v135
	s_waitcnt lgkmcnt(0)
	v_lshl_add_u64 v[102:103], s[16:17], 0, v[10:11]
	v_or_b32_e32 v12, 0x500, v190
	v_or_b32_e32 v16, 0x600, v190
	v_or_b32_e32 v20, 0x700, v190
	v_lshl_add_u64 v[112:113], s[18:19], 0, v[10:11]
	v_lshlrev_b64 v[10:11], 12, v[210:211]
	v_lshlrev_b32_e32 v14, 2, v12
	v_mov_b32_e32 v15, v135
	v_lshlrev_b32_e32 v18, 2, v16
	v_mov_b32_e32 v19, v135
	v_lshlrev_b32_e32 v22, 2, v20
	v_mov_b32_e32 v23, v135
	v_lshl_or_b32 v10, v184, 3, v10
	v_cmp_lt_i32_e32 vcc, v179, v180
	v_and_b32_e32 v3, 0xe0, v182
	v_lshlrev_b32_e32 v5, 4, v140
	v_and_b32_e32 v7, 12, v183
	v_lshl_add_u64 v[110:111], s[18:19], 0, v[134:135]
	v_lshl_add_u64 v[114:115], s[18:19], 0, v[14:15]
	v_lshl_add_u64 v[116:117], s[18:19], 0, v[18:19]
	v_lshl_add_u64 v[118:119], s[18:19], 0, v[22:23]
	v_lshl_add_u64 v[10:11], s[26:27], 0, v[10:11]
	s_mov_b64 s[18:19], 0xe00
	v_cndmask_b32_e32 v1, v178, v179, vcc
	v_cmp_lt_i32_e32 vcc, v181, v180
	v_lshl_add_u64 v[122:123], v[10:11], 0, s[18:19]
	v_or3_b32 v10, v3, v5, v7
	v_mov_b32_e32 v11, v135
	v_cndmask_b32_e32 v2, v178, v181, vcc
	v_lshl_add_u64 v[126:127], s[36:37], 0, v[10:11]
	v_lshlrev_b64 v[10:11], 13, v[210:211]
	v_lshlrev_b32_e32 v185, 2, v2
	s_mov_b32 s24, 1
	v_or_b32_e32 v2, 0x100, v190
	v_or_b32_e32 v4, 0x200, v190
	v_or_b32_e32 v6, 0x300, v190
	v_or_b32_e32 v10, v10, v188
	v_lshl_add_u64 v[98:99], s[28:29], 0, v[190:191]
	s_ashr_i32 s25, s24, 31
	v_lshl_add_u64 v[10:11], s[30:31], 0, v[10:11]
	s_mov_b64 s[28:29], 0x1c0c
	v_lshlrev_b32_e32 v130, 2, v2
	v_lshlrev_b32_e32 v136, 2, v4
	v_lshlrev_b32_e32 v140, 2, v6
	v_lshlrev_b32_e32 v144, 2, v8
	v_lshlrev_b32_e32 v148, 2, v12
	v_lshlrev_b32_e32 v152, 2, v16
	v_lshlrev_b32_e32 v156, 2, v20
	v_lshlrev_b32_e32 v1, 2, v1
	v_lshl_add_u64 v[100:101], s[16:17], 0, v[134:135]
	v_lshl_add_u64 v[104:105], s[16:17], 0, v[14:15]
	v_lshl_add_u64 v[106:107], s[16:17], 0, v[18:19]
	v_lshl_add_u64 v[108:109], s[16:17], 0, v[22:23]
	v_lshlrev_b64 v[120:121], 2, v[210:211]
	s_lshl_b64 s[16:17], s[24:25], 2
	s_lshl_b64 s[18:19], s[24:25], 12
	v_lshlrev_b64 v[124:125], 11, v[210:211]
	s_lshl_b64 s[26:27], s[24:25], 11
	v_lshl_add_u64 v[128:129], v[10:11], 0, s[28:29]
	s_lshl_b64 s[28:29], s[24:25], 13
	s_mov_b64 s[30:31], 0
	v_mov_b32_e32 v183, 0x358637bd
	s_mov_b32 s3, 0x800000
	s_mov_b64 s[36:37], 0x4000
	s_movk_i32 s25, 0xf000
	v_mov_b32_e32 v132, v130
	v_mov_b32_e32 v133, v135
	v_mov_b32_e32 v138, v136
	v_mov_b32_e32 v139, v135
	v_mov_b32_e32 v142, v140
	v_mov_b32_e32 v143, v135
	v_mov_b32_e32 v146, v144
	v_mov_b32_e32 v147, v135
	v_mov_b32_e32 v150, v148
	v_mov_b32_e32 v151, v135
	v_mov_b32_e32 v154, v152
	v_mov_b32_e32 v155, v135
	v_mov_b32_e32 v158, v156
	v_mov_b32_e32 v159, v135
	s_mov_b64 s[38:39], 0x6000
	s_mov_b64 s[40:41], 0x8000
	s_mov_b32 s35, 0x42ee0000
	s_mov_b32 s46, 0xc0c0500
	s_mov_b32 s47, 0xff0000
	s_mov_b32 s50, 0x80808080
	s_mov_b32 s51, 0x8080808
	s_mov_b32 s52, 0xf0f0f0f
	s_movk_i32 s53, 0x1fff
	v_mov_b32_e32 v191, 0xf0f0f0f
	v_mov_b32_e32 v192, v210
	s_branch .LBB0_1127
.LBB0_1126:
	s_or_b64 exec, exec, s[42:43]
	v_add_u32_e32 v192, s24, v192
	v_and_b32_e32 v20, 3, v192
	v_cmp_eq_u32_e32 vcc, 0, v20
	v_lshl_add_u64 v[120:121], v[120:121], 0, s[16:17]
	v_lshl_add_u64 v[122:123], v[122:123], 0, s[18:19]
	v_lshl_add_u64 v[126:127], v[126:127], 0, s[26:27]
	v_lshl_add_u64 v[128:129], v[128:129], 0, s[28:29]
	s_or_b64 s[30:31], vcc, s[30:31]
	v_lshl_add_u64 v[98:99], v[98:99], 0, s[26:27]
	s_andn2_b64 exec, exec, s[30:31]
	s_cbranch_execz .LBB0_1131

; __device__ __forceinline__ unsigned xb_ld(unsigned* p)              { return __hip_atomic_load(p, __ATOMIC_RELAXED, __HIP_MEMORY_SCOPE_AGENT); }
; __device__ __forceinline__ unsigned xb_add(unsigned* p, unsigned v) { return __hip_atomic_fetch_add(p, v, __ATOMIC_RELAXED, __HIP_MEMORY_SCOPE_AGENT); }
; #define XB_SPIN(cond, bar) do { unsigned _sp = 0; while (cond) { __builtin_amdgcn_s_sleep(1); \
;     if ((++_sp & 255u) == 0u) { if (xb_ld(&(bar)[XB_TMO])) break; if (_sp > XB_SPIN_CAP) { atomicAdd(&(bar)[XB_TMO], 1u); break; } } } } while (0)
; __device__ __forceinline__ void xcd_barrier(const XcdBarrier& b) {
;   asm volatile("s_waitcnt vmcnt(0)" ::: "memory");
;   __syncthreads();
;   if (threadIdx.x == 0) {
;     unsigned* bar = b.bar;
;     __builtin_amdgcn_s_waitcnt(0);
;     unsigned nloc = b.st[0], nx = b.st[1];
;     if (nloc == 0u) { xcd_barrier_complete(bar, b.x, nloc, nx); b.st[0] = nloc; b.st[1] = nx; }
;     const unsigned old = xb_add(&bar[XB_XSUB(b.x)], 1u);
;     const unsigned gen = old / nloc;
;     if (old + 1u == (gen + 1u) * nloc) {
;       __builtin_amdgcn_fence(__ATOMIC_RELEASE, "agent");
;       asm volatile("s_waitcnt vmcnt(0)" ::: "memory");
;       const unsigned og = xb_add(&bar[XB_TOP], 1u);
;       const unsigned tg = og / nx;
;       if (og + 1u == (tg + 1u) * nx) xb_add(&bar[XB_TOPGEN], 1u);
;       else XB_SPIN(xb_ld(&bar[XB_TOPGEN]) == tg, bar);
;       __builtin_amdgcn_fence(__ATOMIC_ACQUIRE, "agent");
;       xb_add(&bar[XB_XGEN(b.x)], 1u);
;       asm volatile("s_waitcnt vmcnt(0)" ::: "memory");
;     } else {
;       XB_SPIN(xb_ld(&bar[XB_XGEN(b.x)]) == gen, bar);
;       __builtin_amdgcn_fence(__ATOMIC_ACQUIRE, "agent");
;       asm volatile("s_waitcnt vmcnt(0)" ::: "memory");
;     }
;   }
;   __syncthreads();
; }
.LBB0_1131:
	s_or_b64 exec, exec, s[20:21]
	s_waitcnt vmcnt(0)
	s_barrier
	s_and_saveexec_b64 s[8:9], s[4:5]
	s_cbranch_execz .LBB0_1183
	s_waitcnt vmcnt(0) lgkmcnt(0)
	v_mov_b32_e32 v253, 0x12818
	ds_read_b32 v254, v253 offset:4
	ds_read_b32 v253, v253
	s_waitcnt lgkmcnt(0)
	v_cmp_ne_u32_e32 vcc, 0, v254
	s_cbranch_vccnz .Lmy_gbar_9
	v_readfirstlane_b32 s99, v253
	s_nop 0
	s_and_b32 s100, s99, 7
	s_bfe_u32 s101, s99, 0x30003
	s_lshl_b32 s100, s100, 3
	s_or_b32 s100, s100, s101
	s_and_b32 s101, s100, 31
	s_add_u32 s101, s101, 12
	s_lshl_b32 s101, s101, 8
	s_lshr_b32 s100, s100, 5
	s_lshl_b32 s100, s100, 6
	s_add_u32 s101, s101, s100
	v_mov_b32_e32 v253, s101
	v_mov_b32_e32 v254, 1
	global_atomic_add v253, v254, s[44:45] offset:128
	buffer_inv sc1
	s_mov_b32 s100, 0
.Lmy_gs_w_9:
	global_load_dword v254, v253, s[44:45] offset:128 sc1
	s_waitcnt vmcnt(0)
	v_cmp_le_u32_e32 vcc, 16, v254
	s_cbranch_vccnz .Lgb_wd_9
	s_sleep 1
	s_add_u32 s100, s100, 1
	s_cmp_lt_u32 s100, 0x100000
	s_cbranch_scc1 .Lmy_gs_w_9
	s_branch .Lgb_wd_9

; __device__ __forceinline__ int opaque_tid() { int t = threadIdx.x; asm volatile("" : "+v"(t)); return t; }
; __device__ void phase_q_route(KParams& p, int bid, int nb, char* smem) {
;   const int tid = opaque_tid(), lane = tid & 63, w = tid >> 6;
;   const int wm = w >> 1, wn = w & 1, lr = lane & 15, lq = lane >> 4;
;   const int l31 = lane & 31, lh = lane >> 5;
;   for (int tile0 = bid; tile0 < 512; tile0 += nb) {
;     const int tile = ((nb & 7) == 0 && nb >= 512) ? (((tile0 & 7) * 8 + ((tile0 >> 3) & 7)) * 8 + (tile0 >> 6)) : tile0;
;     const int h = tile & 7, m0 = (tile >> 3) * 128;
.Lgb_wd_9:
.LBB0_1183:
	s_or_b64 exec, exec, s[8:9]
	v_mov_b32_e32 v253, 0x12818
	ds_read_b32 v253, v253
	s_waitcnt lgkmcnt(0)
	v_readfirstlane_b32 s2, v253
	s_nop 0
	s_mov_b64 s[10:11], s[0:1]
	s_waitcnt lgkmcnt(0)
	v_mov_b32_e32 v1, v0
	s_cmpk_gt_i32 s2, 0x1ff
	s_barrier
	s_cbranch_scc1 .LBB0_1196
	s_load_dwordx2 s[20:21], s[10:11], 0xf8
	s_load_dwordx2 s[12:13], s[10:11], 0x108
	v_ashrrev_i32_e32 v2, 1, v1
	s_cmpk_gt_i32 s34, 0x1ff
	v_and_b32_e32 v2, 0xffffffc0, v2
	v_and_b32_e32 v6, 63, v1
	s_cselect_b64 s[8:9], -1, 0
	v_ashrrev_i32_e32 v3, 31, v2
	s_and_b64 s[22:23], s[8:9], s[48:49]
	s_waitcnt lgkmcnt(0)
	v_lshl_add_u64 v[4:5], v[2:3], 2, s[12:13]
	v_lshrrev_b32_e32 v3, 2, v1
	v_cmp_lt_u32_e64 s[8:9], 31, v6
	v_lshrrev_b32_e32 v6, 3, v1
	v_and_b32_e32 v8, 31, v1
	v_ashrrev_i32_e32 v10, 6, v1
	v_and_b32_e32 v11, 12, v3
	v_lshlrev_b32_e32 v12, 3, v1
	s_movk_i32 s3, 0x1100
	v_and_b32_e32 v6, 9, v6
	v_or_b32_e32 v2, v11, v2
	v_and_b32_e32 v76, 8, v12
	v_lshlrev_b32_e32 v12, 8, v8
	v_mul_lo_u32 v14, v10, s3
	s_movk_i32 s3, 0x88
	s_load_dwordx4 s[12:15], s[10:11], 0x138
	s_load_dwordx4 s[16:19], s[10:11], 0x240
	v_or_b32_e32 v16, 2, v6
	v_or_b32_e32 v20, 4, v6
	v_or_b32_e32 v24, 6, v6
	v_bfe_u32 v7, v1, 5, 1
	v_and_b32_e32 v9, 15, v1
	v_lshlrev_b32_e32 v66, 2, v11
	v_mov_b32_e32 v67, 0
	v_lshl_or_b32 v12, v10, 13, v12
	v_and_b32_e32 v13, 7, v1
	v_mad_u32_u24 v78, v8, s3, v14
	v_lshl_or_b32 v79, v10, 5, v8
	v_lshlrev_b32_e32 v2, 8, v2
	v_bitop3_b32 v3, v3, v6, 12 bitop3:0x6c
	v_bitop3_b32 v10, v11, v6, 1 bitop3:0x36
	v_bitop3_b32 v14, v11, v6, 2 bitop3:0x36
	v_bitop3_b32 v15, v11, v6, 3 bitop3:0x36
	v_bitop3_b32 v17, v6, v11, 2 bitop3:0x36
	v_bitop3_b32 v18, v11, v16, 1 bitop3:0x36
	v_bitop3_b32 v19, v11, v6, 2 bitop3:0x14
	v_bitop3_b32 v16, v11, v16, 3 bitop3:0x36
	v_bitop3_b32 v21, v6, v11, 4 bitop3:0x36
	v_bitop3_b32 v22, v11, v20, 1 bitop3:0x36
	v_bitop3_b32 v23, v11, v20, 2 bitop3:0x36
	v_bitop3_b32 v20, v11, v20, 3 bitop3:0x36
	v_bitop3_b32 v6, v6, v11, 6 bitop3:0x36
	v_bitop3_b32 v25, v11, v24, 1 bitop3:0x36
	v_bitop3_b32 v26, v11, v24, 2 bitop3:0x36
	v_bitop3_b32 v11, v11, v24, 3 bitop3:0x36
	v_lshl_add_u64 v[68:69], v[4:5], 0, v[66:67]
	v_lshlrev_b32_e32 v4, 1, v1
	v_lshlrev_b32_e32 v77, 2, v7
	v_lshl_or_b32 v3, v3, 4, v2
	v_lshl_or_b32 v10, v10, 4, v2
	v_lshl_or_b32 v14, v14, 4, v2
	v_lshl_or_b32 v15, v15, 4, v2
	v_lshl_or_b32 v17, v17, 4, v2
	v_lshl_or_b32 v18, v18, 4, v2
	v_lshl_or_b32 v19, v19, 4, v2
	v_lshl_or_b32 v16, v16, 4, v2
	v_lshl_or_b32 v21, v21, 4, v2
	v_lshl_or_b32 v22, v22, 4, v2
	v_lshl_or_b32 v23, v23, 4, v2
	v_lshl_or_b32 v20, v20, 4, v2
	v_lshl_or_b32 v6, v6, 4, v2
	v_lshl_or_b32 v25, v25, 4, v2
	v_lshl_or_b32 v26, v26, 4, v2
	v_lshl_or_b32 v2, v11, 4, v2
	v_bitop3_b32 v11, v7, v1, 15 bitop3:0x78
	v_bitop3_b32 v24, v7, v1, 7 bitop3:0x78
	v_bitop3_b32 v27, v7, v9, 2 bitop3:0x36
	v_bitop3_b32 v28, v7, v13, 2 bitop3:0x36
	v_bitop3_b32 v29, v7, v9, 4 bitop3:0x36
	v_bitop3_b32 v30, v7, v13, 4 bitop3:0x36
	v_bitop3_b32 v31, v7, v9, 6 bitop3:0x36
	v_bitop3_b32 v13, v7, v13, 6 bitop3:0x36
	v_bitop3_b32 v32, v7, v9, 8 bitop3:0x36
	v_bitop3_b32 v33, v7, v9, 10 bitop3:0x36
	v_bitop3_b32 v34, v7, v9, 12 bitop3:0x36
	v_bitop3_b32 v7, v7, v9, 14 bitop3:0x36
	v_and_b32_e32 v4, 14, v4
	v_lshlrev_b32_e32 v5, 2, v9
	v_lshlrev_b32_e32 v8, 7, v8
	v_lshlrev_b32_e32 v11, 4, v11
	v_lshlrev_b32_e32 v24, 4, v24
	v_lshlrev_b32_e32 v27, 4, v27
	v_lshlrev_b32_e32 v28, 4, v28
	v_lshlrev_b32_e32 v29, 4, v29
	v_lshlrev_b32_e32 v30, 4, v30
	v_lshlrev_b32_e32 v31, 4, v31
	v_lshlrev_b32_e32 v13, 4, v13
	v_lshlrev_b32_e32 v32, 4, v32
	v_lshlrev_b32_e32 v33, 4, v33
	v_lshlrev_b32_e32 v34, 4, v34
	v_lshlrev_b32_e32 v7, 4, v7
	v_and_b32_e32 v74, 0x4f, v1
	v_bfe_u32 v75, v1, 1, 3
	v_or_b32_e32 v80, 1, v77
	v_or_b32_e32 v81, 2, v77
	v_or_b32_e32 v82, 3, v77
	v_or_b32_e32 v83, 8, v77
	v_or_b32_e32 v84, 9, v77
	v_or_b32_e32 v85, 10, v77
	v_or_b32_e32 v86, 11, v77
	v_or_b32_e32 v87, 16, v77
	v_or_b32_e32 v88, 17, v77
	v_or_b32_e32 v89, 18, v77
	v_or_b32_e32 v90, 19, v77
	v_or_b32_e32 v91, 24, v77
	v_or_b32_e32 v92, 25, v77
	v_or_b32_e32 v93, 26, v77
	v_or_b32_e32 v94, 27, v77
	v_or_b32_e32 v95, 32, v77
	v_or_b32_e32 v96, 33, v77
	v_or_b32_e32 v97, 35, v77
	v_or_b32_e32 v98, 34, v77
	v_or_b32_e32 v99, 43, v77
	v_or_b32_e32 v100, 42, v77
	v_or_b32_e32 v101, 40, v77
	v_or_b32_e32 v102, 41, v77
	v_or_b32_e32 v103, 59, v77
	v_or_b32_e32 v104, 58, v77
	v_or_b32_e32 v105, 56, v77
	v_or_b32_e32 v106, 57, v77
	v_or_b32_e32 v107, 48, v77
	v_or_b32_e32 v108, 49, v77
	v_or_b32_e32 v109, 51, v77
	v_or_b32_e32 v110, 50, v77
	v_or_b32_e32 v111, 64, v77
	v_or_b32_e32 v112, 0x41, v77
	v_or_b32_e32 v113, 0x43, v77
	v_or_b32_e32 v114, 0x42, v77
	v_or_b32_e32 v115, 0x4b, v77
	v_or_b32_e32 v116, 0x4a, v77
	v_or_b32_e32 v117, 0x48, v77
	v_or_b32_e32 v118, 0x49, v77
	v_or_b32_e32 v119, 0x5b, v77
	v_or_b32_e32 v120, 0x5a, v77
	v_or_b32_e32 v121, 0x58, v77
	v_or_b32_e32 v122, 0x59, v77
	v_or_b32_e32 v123, 0x50, v77
	v_or_b32_e32 v124, 0x51, v77
	v_or_b32_e32 v125, 0x53, v77
	v_or_b32_e32 v126, 0x52, v77
	v_or_b32_e32 v127, 0x60, v77
	v_or_b32_e32 v128, 0x61, v77
	v_or_b32_e32 v129, 0x63, v77
	v_or_b32_e32 v130, 0x62, v77
	v_or_b32_e32 v131, 0x6b, v77
	v_or_b32_e32 v132, 0x6a, v77
	v_or_b32_e32 v133, 0x68, v77
	v_or_b32_e32 v134, 0x69, v77
	v_or_b32_e32 v135, 0x7b, v77
	v_or_b32_e32 v136, 0x7a, v77
	v_or_b32_e32 v137, 0x78, v77
	v_or_b32_e32 v138, 0x79, v77
	v_or_b32_e32 v139, 0x70, v77
	v_or_b32_e32 v140, 0x71, v77
	v_or_b32_e32 v141, 0x73, v77
	v_or_b32_e32 v142, 0x72, v77
	s_movk_i32 s3, 0xff80
	s_mov_b64 s[24:25], 0x10000
	s_mov_b64 s[26:27], 0x20000
	s_mov_b64 s[28:29], 0x30000
	s_mov_b32 s35, 0x1ffffc0
	s_mov_b64 s[30:31], 0x80
	s_mov_b64 s[36:37], 0x10080
	s_mov_b64 s[38:39], 0x20080
	s_mov_b64 s[40:41], 0x30080
	v_add_u32_e32 v143, v3, v4
	v_add_u32_e32 v144, v10, v4
	v_add_u32_e32 v145, v14, v4
	v_add_u32_e32 v146, v15, v4
	v_add_u32_e32 v147, v17, v4
	v_add_u32_e32 v148, v18, v4
	v_add_u32_e32 v149, v19, v4
	v_add_u32_e32 v150, v16, v4
	v_add_u32_e32 v151, v21, v4
	v_add_u32_e32 v152, v22, v4
	v_add_u32_e32 v153, v23, v4
	v_add_u32_e32 v154, v20, v4
	v_add_u32_e32 v155, v6, v4
	v_add_u32_e32 v156, v25, v4
	v_add_u32_e32 v157, v26, v4
	v_add_u32_e32 v158, v2, v4
	s_movk_i32 s46, 0x80
	v_lshlrev_b32_e32 v159, 2, v5
	v_add_u32_e32 v160, v12, v11
	v_add_u32_e32 v161, v24, v8
	v_add_u32_e32 v162, v12, v27
	v_add_u32_e32 v163, v28, v8
	v_add_u32_e32 v164, v12, v29
	v_add_u32_e32 v165, v30, v8
	v_add_u32_e32 v166, v12, v31
	v_add_u32_e32 v167, v13, v8
	v_add_u32_e32 v168, v12, v32
	v_add_u32_e32 v169, v12, v33
	v_add_u32_e32 v170, v12, v34
	v_add_u32_e32 v171, v12, v7
	s_movk_i32 s47, 0xff00
	v_mov_b32_e32 v172, 0xc0
	v_mov_b32_e32 v173, 0xb8
	v_bfrev_b32_e32 v174, 1
	s_branch .LBB0_1186
